# attention loops: negm used directly as MFMA srcC (48 v_mov_b64 per tile pair removed)
# speedup vs baseline: 1.0090x; 1.0090x over previous
.LBB0_719:
	s_mul_i32 s26, s64, 0x5400
	s_add_i32 s26, s26, 0
	v_add_u32_e32 v2, s26, v205
	v_and_b32_e32 v4, 64, v242
	v_add_u32_e32 v17, 64, v4
	s_waitcnt lgkmcnt(3)
	ds_read_b128 v[4:7], v2
	s_waitcnt lgkmcnt(1)
	ds_read_b128 v[8:11], v2 offset:32
	ds_read_b128 v[12:15], v2 offset:6656
	ds_read_b128 v[82:85], v2 offset:6688
	ds_read_b128 v[158:161], v2 offset:64
	ds_read_b128 v[162:165], v2 offset:96
	ds_read_b128 v[86:89], v2 offset:6720
	ds_read_b128 v[90:93], v2 offset:6752
	ds_read_b128 v[194:197], v2 offset:128
	ds_read_b128 v[208:211], v2 offset:160
	ds_read_b128 v[94:97], v2 offset:6784
	ds_read_b128 v[166:169], v2 offset:6816
	v_xor_b32_e32 v16, 32, v242
	v_cmp_lt_i32_e32 vcc, v16, v17
	s_nop 1
	v_cndmask_b32_e32 v2, v242, v16, vcc
	v_lshlrev_b32_e32 v16, 2, v2
	v_add_u32_e32 v2, s26, v206
	s_waitcnt lgkmcnt(9)
	v_mfma_f32_32x32x16_bf16 v[66:81], v[12:15], v[134:137], v[50:65]
	s_waitcnt lgkmcnt(8)
	v_mfma_f32_32x32x16_bf16 v[66:81], v[82:85], v[138:141], v[66:81]
	s_waitcnt lgkmcnt(5)
	v_mfma_f32_32x32x16_bf16 v[66:81], v[86:89], v[142:145], v[66:81]
	s_waitcnt lgkmcnt(4)
	v_mfma_f32_32x32x16_bf16 v[66:81], v[90:93], v[146:149], v[66:81]
	s_waitcnt lgkmcnt(1)
	v_mfma_f32_32x32x16_bf16 v[66:81], v[94:97], v[150:153], v[66:81]
	s_waitcnt lgkmcnt(0)
	v_mfma_f32_32x32x16_bf16 v[66:81], v[166:169], v[154:157], v[66:81]
	v_mfma_f32_32x32x16_bf16 v[82:97], v[4:7], v[134:137], v[50:65]
	v_mfma_f32_32x32x16_bf16 v[82:97], v[8:11], v[138:141], v[82:97]
	ds_read_b64_tr_b16 v[174:175], v2 offset:13312
	ds_read_b64_tr_b16 v[176:177], v2 offset:13824
	ds_read_b64_tr_b16 v[170:171], v2 offset:14336
	ds_read_b64_tr_b16 v[172:173], v2 offset:14848
	ds_read_b64_tr_b16 v[166:167], v2 offset:15360
	ds_read_b64_tr_b16 v[168:169], v2 offset:15872
	ds_read_b64_tr_b16 v[8:9], v2 offset:16384
	ds_read_b64_tr_b16 v[10:11], v2 offset:16896
	v_mfma_f32_32x32x16_bf16 v[82:97], v[158:161], v[142:145], v[82:97]
	v_mfma_f32_32x32x16_bf16 v[82:97], v[162:165], v[146:149], v[82:97]
	ds_read_b64_tr_b16 v[162:163], v2 offset:17408
	ds_read_b64_tr_b16 v[164:165], v2 offset:17920
	ds_read_b64_tr_b16 v[158:159], v2 offset:18432
	ds_read_b64_tr_b16 v[160:161], v2 offset:18944
	ds_read_b64_tr_b16 v[12:13], v2 offset:19456
	ds_read_b64_tr_b16 v[14:15], v2 offset:19968
	ds_read_b64_tr_b16 v[4:5], v2 offset:20480
	ds_read_b64_tr_b16 v[6:7], v2 offset:20992
	v_mfma_f32_32x32x16_bf16 v[82:97], v[194:197], v[150:153], v[82:97]
	v_mfma_f32_32x32x16_bf16 v[82:97], v[208:211], v[154:157], v[82:97]
	s_nop 11
	v_max3_f32 v2, v82, v83, v84
	v_max3_f32 v194, v66, v67, v68
	v_max3_f32 v2, v2, v85, v86
	v_max3_f32 v194, v194, v69, v70
	v_max3_f32 v2, v2, v87, v88
	v_max3_f32 v194, v194, v71, v72
	v_max3_f32 v2, v2, v89, v90
	v_max3_f32 v194, v194, v73, v74
	v_max3_f32 v2, v2, v91, v92
	v_max3_f32 v194, v194, v75, v76
	v_max3_f32 v2, v2, v93, v94
	v_max3_f32 v194, v194, v77, v78
	v_max_f32_e32 v195, v81, v81
	v_max_f32_e32 v196, v97, v97
	v_max3_f32 v2, v2, v95, v96
	v_max3_f32 v194, v194, v79, v80
	v_max_f32_e32 v195, v196, v195
	v_max3_f32 v2, v2, v194, v195
	ds_bpermute_b32 v194, v16, v2
	s_cmp_lg_u32 s73, 0
	s_waitcnt lgkmcnt(0)
	v_max_f32_e32 v194, v194, v194
	v_max_f32_e32 v208, v2, v194
	s_cbranch_scc0 .LBB0_731
	v_cmp_lt_f32_e32 vcc, s81, v208
	s_mov_b64 s[28:29], 0
	s_mov_b64 s[26:27], 0
	s_cbranch_vccz .LBB0_722
	v_max_f32_e32 v2, v208, v208
	v_max_f32_e32 v2, 0, v2
	s_mov_b64 s[26:27], -1

.LBB0_756:
	v_and_b32_e32 v5, 64, v242
	s_mul_i32 s26, s64, 0x5400
	v_xor_b32_e32 v4, 32, v242
	v_add_u32_e32 v5, 64, v5
	s_add_i32 s26, s26, 0
	v_cmp_lt_i32_e32 vcc, v4, v5
	v_add_u32_e32 v2, s26, v205
	s_nop 0
	v_cndmask_b32_e32 v4, v242, v4, vcc
	v_lshlrev_b32_e32 v222, 2, v4
	s_waitcnt lgkmcnt(3)
	ds_read_b128 v[4:7], v2 offset:6656
	s_waitcnt lgkmcnt(1)
	ds_read_b128 v[8:11], v2
	ds_read_b128 v[12:15], v2 offset:32
	ds_read_b128 v[158:161], v2 offset:6688
	ds_read_b128 v[162:165], v2 offset:64
	ds_read_b128 v[166:169], v2 offset:6720
	ds_read_b128 v[170:173], v2 offset:96
	ds_read_b128 v[174:177], v2 offset:6752
	ds_read_b128 v[194:197], v2 offset:128
	ds_read_b128 v[210:213], v2 offset:6784
	ds_read_b128 v[214:217], v2 offset:160
	ds_read_b128 v[218:221], v2 offset:6816
	v_subrev_u32_e32 v2, 59, v209
	s_waitcnt lgkmcnt(10)
	v_mfma_f32_32x32x16_bf16 v[82:97], v[8:11], v[134:137], v[50:65]
	v_mfma_f32_32x32x16_bf16 v[66:81], v[4:7], v[134:137], v[50:65]
	v_add_u32_e32 v6, s26, v206
	s_waitcnt lgkmcnt(9)
	v_mfma_f32_32x32x16_bf16 v[82:97], v[12:15], v[138:141], v[82:97]
	s_waitcnt lgkmcnt(8)
	v_mfma_f32_32x32x16_bf16 v[66:81], v[158:161], v[138:141], v[66:81]
	s_waitcnt lgkmcnt(7)
	v_mfma_f32_32x32x16_bf16 v[82:97], v[162:165], v[142:145], v[82:97]
	s_waitcnt lgkmcnt(6)
	v_mfma_f32_32x32x16_bf16 v[66:81], v[166:169], v[142:145], v[66:81]
	s_waitcnt lgkmcnt(5)
	v_mfma_f32_32x32x16_bf16 v[82:97], v[170:173], v[146:149], v[82:97]
	s_waitcnt lgkmcnt(4)
	v_mfma_f32_32x32x16_bf16 v[66:81], v[174:177], v[146:149], v[66:81]
	ds_read_b64_tr_b16 v[174:175], v6 offset:13312
	ds_read_b64_tr_b16 v[176:177], v6 offset:13824
	ds_read_b64_tr_b16 v[170:171], v6 offset:14336
	ds_read_b64_tr_b16 v[172:173], v6 offset:14848
	ds_read_b64_tr_b16 v[166:167], v6 offset:15360
	ds_read_b64_tr_b16 v[168:169], v6 offset:15872
	ds_read_b64_tr_b16 v[162:163], v6 offset:16384
	ds_read_b64_tr_b16 v[164:165], v6 offset:16896
	ds_read_b64_tr_b16 v[158:159], v6 offset:17408
	ds_read_b64_tr_b16 v[160:161], v6 offset:17920
	ds_read_b64_tr_b16 v[12:13], v6 offset:18432
	ds_read_b64_tr_b16 v[14:15], v6 offset:18944
	ds_read_b64_tr_b16 v[8:9], v6 offset:19456
	ds_read_b64_tr_b16 v[10:11], v6 offset:19968
	ds_read_b64_tr_b16 v[4:5], v6 offset:20480
	ds_read_b64_tr_b16 v[6:7], v6 offset:20992
	s_waitcnt lgkmcnt(14)
	v_mfma_f32_32x32x16_bf16 v[82:97], v[194:197], v[150:153], v[82:97]
	v_mfma_f32_32x32x16_bf16 v[66:81], v[210:213], v[150:153], v[66:81]
	v_mfma_f32_32x32x16_bf16 v[82:97], v[214:217], v[154:157], v[82:97]
	v_mfma_f32_32x32x16_bf16 v[66:81], v[218:221], v[154:157], v[66:81]
	v_subrev_u32_e32 v16, 27, v209
	v_cmp_le_i32_e32 vcc, v16, v208
	s_cmp_lg_u32 s35, -1
	s_nop 8
	v_cndmask_b32_e32 v16, v243, v66, vcc
	v_cmp_lt_i32_e32 vcc, v2, v208
	s_nop 1
	v_cndmask_b32_e32 v83, v243, v83, vcc
	v_cmp_le_i32_e32 vcc, v2, v208
	v_subrev_u32_e32 v2, 26, v209
	s_nop 0
	v_cndmask_b32_e32 v82, v243, v82, vcc
	v_cmp_le_i32_e32 vcc, v2, v208
	v_subrev_u32_e32 v2, 57, v209
	s_nop 0
	v_cndmask_b32_e32 v17, v243, v67, vcc
	v_cmp_le_i32_e32 vcc, v2, v208
	v_subrev_u32_e32 v2, 25, v209
	s_nop 0
	v_cndmask_b32_e32 v66, v243, v84, vcc
	v_cmp_le_i32_e32 vcc, v2, v208
	v_subrev_u32_e32 v2, 56, v209
	s_nop 0
	v_cndmask_b32_e32 v68, v243, v68, vcc
	v_cmp_le_i32_e32 vcc, v2, v208
	v_subrev_u32_e32 v2, 24, v209
	s_nop 0
	v_cndmask_b32_e32 v67, v243, v85, vcc
	v_cmp_le_i32_e32 vcc, v2, v208
	v_subrev_u32_e32 v2, 51, v209
	s_nop 0
	v_cndmask_b32_e32 v69, v243, v69, vcc
	v_cmp_le_i32_e32 vcc, v2, v208
	v_subrev_u32_e32 v2, 19, v209
	s_nop 0
	v_cndmask_b32_e32 v84, v243, v86, vcc
	v_cmp_le_i32_e32 vcc, v2, v208
	v_subrev_u32_e32 v2, 50, v209
	s_nop 0
	v_cndmask_b32_e32 v70, v243, v70, vcc
	v_cmp_le_i32_e32 vcc, v2, v208
	v_subrev_u32_e32 v2, 18, v209
	s_nop 0
	v_cndmask_b32_e32 v85, v243, v87, vcc
	v_cmp_le_i32_e32 vcc, v2, v208
	v_subrev_u32_e32 v2, 49, v209
	s_nop 0
	v_cndmask_b32_e32 v71, v243, v71, vcc
	v_cmp_le_i32_e32 vcc, v2, v208
	v_subrev_u32_e32 v2, 17, v209
	s_nop 0
	v_cndmask_b32_e32 v86, v243, v88, vcc
	v_cmp_le_i32_e32 vcc, v2, v208
	v_subrev_u32_e32 v2, 48, v209
	s_nop 0
	v_cndmask_b32_e32 v72, v243, v72, vcc
	v_cmp_le_i32_e32 vcc, v2, v208
	v_add_u32_e32 v2, -16, v209
	s_nop 0
	v_cndmask_b32_e32 v87, v243, v89, vcc
	v_cmp_le_i32_e32 vcc, v2, v208
	v_subrev_u32_e32 v2, 43, v209
	s_nop 0
	v_cndmask_b32_e32 v73, v243, v73, vcc
	v_cmp_le_i32_e32 vcc, v2, v208
	v_add_u32_e32 v2, -11, v209
	s_nop 0
	v_cndmask_b32_e32 v88, v243, v90, vcc
	v_cmp_le_i32_e32 vcc, v2, v208
	v_subrev_u32_e32 v2, 42, v209
	s_nop 0
	v_cndmask_b32_e32 v74, v243, v74, vcc
	v_cmp_le_i32_e32 vcc, v2, v208
	v_add_u32_e32 v2, -10, v209
	s_nop 0
	v_cndmask_b32_e32 v89, v243, v91, vcc
	v_cmp_le_i32_e32 vcc, v2, v208
	v_subrev_u32_e32 v2, 41, v209
	s_nop 0
	v_cndmask_b32_e32 v75, v243, v75, vcc
	v_cmp_le_i32_e32 vcc, v2, v208
	v_add_u32_e32 v2, -9, v209
	s_nop 0
	v_cndmask_b32_e32 v90, v243, v92, vcc
	v_cmp_le_i32_e32 vcc, v2, v208
	v_subrev_u32_e32 v2, 40, v209
	s_nop 0
	v_cndmask_b32_e32 v76, v243, v76, vcc
	v_cmp_le_i32_e32 vcc, v2, v208
	v_add_u32_e32 v2, -8, v209
	s_nop 0
	v_cndmask_b32_e32 v91, v243, v93, vcc
	v_cmp_le_i32_e32 vcc, v2, v208
	v_subrev_u32_e32 v2, 35, v209
	s_nop 0
	v_cndmask_b32_e32 v77, v243, v77, vcc
	v_cmp_le_i32_e32 vcc, v2, v208
	v_add_u32_e32 v2, -3, v209
	s_nop 0
	v_cndmask_b32_e32 v92, v243, v94, vcc
	v_cmp_le_i32_e32 vcc, v2, v208
	v_subrev_u32_e32 v2, 34, v209
	s_nop 0
	v_cndmask_b32_e32 v78, v243, v78, vcc
	v_cmp_le_i32_e32 vcc, v2, v208
	v_add_u32_e32 v2, -2, v209
	s_nop 0
	v_cndmask_b32_e32 v93, v243, v95, vcc
	v_cmp_le_i32_e32 vcc, v2, v208
	v_subrev_u32_e32 v2, 33, v209
	s_nop 0
	v_cndmask_b32_e32 v79, v243, v79, vcc
	v_cmp_le_i32_e32 vcc, v2, v208
	v_add_u32_e32 v2, -1, v209
	s_nop 0
	v_cndmask_b32_e32 v94, v243, v96, vcc
	v_cmp_le_i32_e32 vcc, v2, v208
	v_subrev_u32_e32 v2, 32, v209
	v_max3_f32 v96, v16, v17, v68
	v_cndmask_b32_e32 v80, v243, v80, vcc
	v_cmp_le_i32_e32 vcc, v2, v208
	v_max3_f32 v2, v82, v83, v66
	v_max3_f32 v2, v2, v67, v84
	v_max3_f32 v96, v96, v69, v70
	v_max3_f32 v2, v2, v85, v86
	v_max3_f32 v96, v96, v71, v72
	v_cndmask_b32_e32 v95, v243, v97, vcc
	v_cmp_le_i32_e32 vcc, v209, v208
	v_max3_f32 v2, v2, v87, v88
	v_max3_f32 v96, v96, v73, v74
	v_cndmask_b32_e32 v81, v243, v81, vcc
	v_max3_f32 v2, v2, v89, v90
	v_max3_f32 v96, v96, v75, v76
	v_max3_f32 v2, v2, v91, v92
	v_max3_f32 v96, v96, v77, v78
	v_max_f32_e32 v97, v81, v81
	v_max_f32_e32 v194, v95, v95
	v_max3_f32 v2, v2, v93, v94
	v_max3_f32 v96, v96, v79, v80
	v_max_f32_e32 v97, v194, v97
	v_max3_f32 v2, v2, v96, v97
	ds_bpermute_b32 v96, v222, v2
	s_waitcnt lgkmcnt(0)
	v_max_f32_e32 v96, v96, v96
	v_max_f32_e32 v96, v2, v96
	s_cbranch_scc0 .LBB0_763
	v_cmp_lt_f32_e32 vcc, s81, v96
	s_mov_b64 s[26:27], 0
	s_cbranch_vccz .LBB0_759
	v_max_f32_e32 v2, v96, v96
	v_max_f32_e32 v2, 0, v2
	s_mov_b64 s[10:11], -1

.LBB0_851:
	s_mul_i32 s2, s74, 0x4400
	s_add_i32 s6, s2, 0
	v_add_u32_e32 v5, s6, v207
	ds_read_b128 v[6:9], v5 offset:4608
	ds_read_b128 v[10:13], v5
	ds_read_b128 v[14:17], v5 offset:32
	ds_read_b128 v[146:149], v5 offset:4640
	v_and_b32_e32 v4, 64, v242
	v_xor_b32_e32 v2, 32, v242
	v_add_u32_e32 v4, 64, v4
	v_cmp_lt_i32_e32 vcc, v2, v4
	s_cmp_lg_u32 s10, 0
	s_cselect_b64 s[2:3], -1, 0
	v_cndmask_b32_e32 v2, v242, v2, vcc
	v_lshlrev_b32_e32 v4, 2, v2
	s_waitcnt lgkmcnt(2)
	v_mfma_f32_32x32x16_bf16 v[130:145], v[10:13], v[178:181], v[98:113]
	s_and_b64 vcc, exec, s[2:3]
	v_mfma_f32_32x32x16_bf16 v[114:129], v[6:9], v[178:181], v[98:113]
	s_waitcnt lgkmcnt(1)
	v_mfma_f32_32x32x16_bf16 v[130:145], v[14:17], v[182:185], v[130:145]
	s_waitcnt lgkmcnt(0)
	v_mfma_f32_32x32x16_bf16 v[114:129], v[146:149], v[182:185], v[114:129]
	s_nop 9
	v_max3_f32 v2, v130, v131, v132
	v_max3_f32 v2, v2, v133, v134
	v_max3_f32 v2, v2, v135, v136
	v_max3_f32 v2, v2, v137, v138
	v_max3_f32 v2, v2, v139, v140
	v_max3_f32 v2, v2, v141, v142
	v_max_f32_e32 v8, v145, v145
	v_max3_f32 v6, v114, v115, v116
	v_max3_f32 v6, v6, v117, v118
	v_max3_f32 v6, v6, v119, v120
	v_max3_f32 v6, v6, v121, v122
	v_max3_f32 v6, v6, v123, v124
	v_max3_f32 v6, v6, v125, v126
	v_max_f32_e32 v7, v129, v129
	v_max3_f32 v2, v2, v143, v144
	v_max3_f32 v6, v6, v127, v128
	v_max_f32_e32 v7, v8, v7
	v_max3_f32 v2, v2, v6, v7
	ds_bpermute_b32 v6, v4, v2
	s_waitcnt lgkmcnt(0)
	v_max_f32_e32 v6, v6, v6
	v_max_f32_e32 v6, v2, v6
	s_cbranch_vccz .LBB0_865
	v_cmp_lt_f32_e32 vcc, s11, v6
	s_mov_b64 s[4:5], 0
	s_cbranch_vccz .LBB0_854
	v_max_f32_e32 v2, v6, v6
	v_max_f32_e32 v2, 0, v2
	s_mov_b64 s[0:1], -1

.LBB0_858:
	ds_read_b128 v[6:9], v5 offset:64
	ds_read_b128 v[10:13], v5 offset:96
	ds_read_b128 v[14:17], v5 offset:4672
	ds_read_b128 v[194:197], v5 offset:4704
	s_waitcnt lgkmcnt(3)
	v_mfma_f32_32x32x16_bf16 v[162:177], v[6:9], v[186:189], v[82:97]
	s_and_b64 vcc, exec, s[2:3]
	s_waitcnt lgkmcnt(1)
	v_mfma_f32_32x32x16_bf16 v[146:161], v[14:17], v[186:189], v[82:97]
	v_mfma_f32_32x32x16_bf16 v[162:177], v[10:13], v[190:193], v[162:177]
	s_waitcnt lgkmcnt(0)
	v_mfma_f32_32x32x16_bf16 v[146:161], v[194:197], v[190:193], v[146:161]
	s_nop 9
	v_max3_f32 v2, v162, v163, v164
	v_max3_f32 v2, v2, v165, v166
	v_max3_f32 v2, v2, v167, v168
	v_max3_f32 v2, v2, v169, v170
	v_max3_f32 v2, v2, v171, v172
	v_max3_f32 v2, v2, v173, v174
	v_max_f32_e32 v7, v177, v177
	v_max3_f32 v5, v146, v147, v148
	v_max3_f32 v5, v5, v149, v150
	v_max3_f32 v5, v5, v151, v152
	v_max3_f32 v5, v5, v153, v154
	v_max3_f32 v5, v5, v155, v156
	v_max3_f32 v5, v5, v157, v158
	v_max_f32_e32 v6, v161, v161
	v_max3_f32 v2, v2, v175, v176
	v_max3_f32 v5, v5, v159, v160
	v_max_f32_e32 v6, v7, v6
	v_max3_f32 v2, v2, v5, v6
	ds_bpermute_b32 v4, v4, v2
	s_waitcnt lgkmcnt(0)
	v_max_f32_e32 v4, v4, v4
	v_max_f32_e32 v4, v2, v4
	s_cbranch_vccz .LBB0_866
	v_cmp_lt_f32_e32 vcc, s11, v4
	s_mov_b64 s[2:3], 0
	s_mov_b64 s[0:1], 0
	s_cbranch_vccz .LBB0_861
	v_max_f32_e32 v2, v4, v4
	v_max_f32_e32 v2, 0, v2
	s_mov_b64 s[0:1], -1

.LBB0_883:
	v_and_b32_e32 v5, 64, v242
	s_mul_i32 s2, s74, 0x4400
	v_xor_b32_e32 v4, 32, v242
	v_add_u32_e32 v5, 64, v5
	s_add_i32 s83, s2, 0
	v_cmp_lt_i32_e32 vcc, v4, v5
	v_add_u32_e32 v164, s83, v207
	s_cmp_lg_u32 s82, -1
	v_cndmask_b32_e32 v4, v242, v4, vcc
	v_lshlrev_b32_e32 v217, 2, v4
	ds_read_b128 v[4:7], v164 offset:4608
	ds_read_b128 v[8:11], v164
	ds_read_b128 v[12:15], v164 offset:32
	ds_read_b128 v[146:149], v164 offset:4640
	s_cselect_b64 s[88:89], -1, 0
	v_subrev_u32_e32 v2, 59, v177
	v_cmp_gt_i32_e64 s[2:3], v2, v176
	v_cmp_lt_i32_e64 s[6:7], v2, v176
	v_subrev_u32_e32 v2, 26, v177
	v_cmp_gt_i32_e64 s[8:9], v2, v176
	v_subrev_u32_e32 v2, 57, v177
	v_cmp_gt_i32_e64 s[10:11], v2, v176
	v_subrev_u32_e32 v2, 25, v177
	v_cmp_gt_i32_e64 s[12:13], v2, v176
	v_subrev_u32_e32 v2, 56, v177
	v_cmp_gt_i32_e64 s[14:15], v2, v176
	v_subrev_u32_e32 v2, 24, v177
	v_cmp_gt_i32_e64 s[16:17], v2, v176
	v_subrev_u32_e32 v2, 51, v177
	v_cmp_gt_i32_e64 s[18:19], v2, v176
	v_subrev_u32_e32 v2, 19, v177
	v_cmp_gt_i32_e64 s[20:21], v2, v176
	v_subrev_u32_e32 v2, 50, v177
	v_cmp_gt_i32_e64 s[22:23], v2, v176
	v_subrev_u32_e32 v2, 18, v177
	v_cmp_gt_i32_e64 s[24:25], v2, v176
	v_subrev_u32_e32 v2, 49, v177
	s_waitcnt lgkmcnt(2)
	v_mfma_f32_32x32x16_bf16 v[130:145], v[8:11], v[178:181], v[98:113]
	v_cmp_gt_i32_e64 s[26:27], v2, v176
	v_subrev_u32_e32 v2, 17, v177
	v_mfma_f32_32x32x16_bf16 v[114:129], v[4:7], v[178:181], v[98:113]
	v_cmp_gt_i32_e64 s[28:29], v2, v176
	v_subrev_u32_e32 v2, 48, v177
	v_cmp_gt_i32_e64 s[30:31], v2, v176
	v_add_u32_e32 v2, -16, v177
	v_cmp_gt_i32_e64 s[34:35], v2, v176
	v_subrev_u32_e32 v2, 43, v177
	v_cmp_gt_i32_e64 s[36:37], v2, v176
	v_add_u32_e32 v2, -11, v177
	v_cmp_gt_i32_e64 s[38:39], v2, v176
	v_subrev_u32_e32 v2, 42, v177
	v_cmp_gt_i32_e64 s[40:41], v2, v176
	v_add_u32_e32 v2, -10, v177
	v_cmp_gt_i32_e64 s[42:43], v2, v176
	v_subrev_u32_e32 v2, 41, v177
	s_waitcnt lgkmcnt(1)
	v_mfma_f32_32x32x16_bf16 v[130:145], v[12:15], v[182:185], v[130:145]
	v_cmp_gt_i32_e64 s[44:45], v2, v176
	v_add_u32_e32 v2, -9, v177
	v_cmp_gt_i32_e64 s[46:47], v2, v176
	v_subrev_u32_e32 v2, 40, v177
	v_cmp_gt_i32_e64 s[48:49], v2, v176
	v_add_u32_e32 v2, -8, v177
	v_cmp_gt_i32_e64 s[50:51], v2, v176
	s_waitcnt lgkmcnt(0)
	v_mfma_f32_32x32x16_bf16 v[114:129], v[146:149], v[182:185], v[114:129]
	v_subrev_u32_e32 v2, 35, v177
	v_cmp_gt_i32_e64 s[52:53], v2, v176
	v_add_u32_e32 v2, -3, v177
	v_cmp_gt_i32_e64 s[54:55], v2, v176
	v_subrev_u32_e32 v2, 34, v177
	v_cmp_gt_i32_e64 s[56:57], v2, v176
	v_add_u32_e32 v2, -2, v177
	v_subrev_u32_e32 v5, 27, v177
	v_cmp_gt_i32_e64 s[58:59], v2, v176
	v_subrev_u32_e32 v2, 33, v177
	v_cndmask_b32_e64 v4, v130, v243, s[2:3]
	v_cmp_gt_i32_e64 s[4:5], v5, v176
	v_cmp_gt_i32_e64 s[60:61], v2, v176
	v_add_u32_e32 v2, -1, v177
	v_cndmask_b32_e64 v160, v114, v243, s[4:5]
	v_cndmask_b32_e64 v162, v4, v130, s[6:7]
	v_cndmask_b32_e64 v163, v243, v131, s[6:7]
	v_cndmask_b32_e64 v161, v115, v243, s[8:9]
	v_cndmask_b32_e64 v156, v132, v243, s[10:11]
	v_cndmask_b32_e64 v158, v116, v243, s[12:13]
	v_cmp_gt_i32_e64 s[62:63], v2, v176
	v_subrev_u32_e32 v2, 32, v177
	v_cndmask_b32_e64 v157, v133, v243, s[14:15]
	v_cndmask_b32_e64 v159, v117, v243, s[16:17]
	v_cndmask_b32_e64 v152, v134, v243, s[18:19]
	v_cndmask_b32_e64 v154, v118, v243, s[20:21]
	v_cmp_gt_i32_e64 s[64:65], v2, v176
	v_max3_f32 v2, v162, v163, v156
	v_max3_f32 v114, v160, v161, v158
	v_cndmask_b32_e64 v153, v135, v243, s[22:23]
	v_cndmask_b32_e64 v155, v119, v243, s[24:25]
	v_cndmask_b32_e64 v148, v136, v243, s[26:27]
	v_cndmask_b32_e64 v150, v120, v243, s[28:29]
	v_max3_f32 v2, v2, v157, v152
	v_max3_f32 v114, v114, v159, v154
	v_cndmask_b32_e64 v149, v137, v243, s[30:31]
	v_cndmask_b32_e64 v151, v121, v243, s[34:35]
	v_cndmask_b32_e64 v10, v138, v243, s[36:37]
	v_cndmask_b32_e64 v146, v122, v243, s[38:39]
	v_max3_f32 v2, v2, v153, v148
	v_max3_f32 v114, v114, v155, v150
	v_cndmask_b32_e64 v11, v139, v243, s[40:41]
	v_cndmask_b32_e64 v147, v123, v243, s[42:43]
	v_cndmask_b32_e64 v8, v140, v243, s[44:45]
	v_cndmask_b32_e64 v12, v124, v243, s[46:47]
	v_cmp_gt_i32_e64 s[66:67], v177, v176
	v_max3_f32 v2, v2, v149, v10
	v_max3_f32 v114, v114, v151, v146
	v_cndmask_b32_e64 v9, v141, v243, s[48:49]
	v_cndmask_b32_e64 v13, v125, v243, s[50:51]
	v_cndmask_b32_e64 v4, v142, v243, s[52:53]
	v_cndmask_b32_e64 v14, v126, v243, s[54:55]
	v_cndmask_b32_e64 v7, v145, v243, s[64:65]
	v_cndmask_b32_e64 v17, v129, v243, s[66:67]
	v_max3_f32 v2, v2, v11, v8
	v_max3_f32 v114, v114, v147, v12
	v_cndmask_b32_e64 v5, v143, v243, s[56:57]
	v_cndmask_b32_e64 v15, v127, v243, s[58:59]
	v_cndmask_b32_e64 v6, v144, v243, s[60:61]
	v_cndmask_b32_e64 v16, v128, v243, s[62:63]
	v_max3_f32 v2, v2, v9, v4
	v_max3_f32 v114, v114, v13, v14
	v_max_f32_e32 v115, v17, v17
	v_max_f32_e32 v116, v7, v7
	v_max3_f32 v2, v2, v5, v6
	v_max3_f32 v114, v114, v15, v16
	v_max_f32_e32 v115, v116, v115
	v_max3_f32 v2, v2, v114, v115
	ds_bpermute_b32 v114, v217, v2
	s_and_b64 vcc, exec, s[88:89]
	s_waitcnt lgkmcnt(0)
	v_max_f32_e32 v114, v114, v114
	v_max_f32_e32 v114, v2, v114
	s_cbranch_vccz .LBB0_897
	v_cmp_lt_f32_e32 vcc, s94, v114
	s_mov_b64 s[94:95], 0
	s_cbranch_vccz .LBB0_886
	v_max_f32_e32 v2, v114, v114
	v_max_f32_e32 v2, 0, v2
	s_mov_b64 s[0:1], -1

.LBB0_890:
	ds_read_b128 v[130:133], v164 offset:64
	ds_read_b128 v[166:169], v164 offset:96
	ds_read_b128 v[170:173], v164 offset:4672
	ds_read_b128 v[194:197], v164 offset:4704
	s_mov_b32 s85, 0x800000
	s_mov_b32 s0, 0x41800000
	s_waitcnt lgkmcnt(3)
	v_mfma_f32_32x32x16_bf16 v[114:129], v[130:133], v[186:189], v[82:97]
	s_waitcnt lgkmcnt(2)
	v_mfma_f32_32x32x16_bf16 v[114:129], v[166:169], v[190:193], v[114:129]
	s_and_b64 vcc, exec, s[88:89]
	s_waitcnt lgkmcnt(1)
	v_mfma_f32_32x32x16_bf16 v[130:145], v[170:173], v[186:189], v[82:97]
	s_nop 8
	v_cndmask_b32_e64 v2, v114, v243, s[2:3]
	v_cndmask_b32_e64 v174, v2, v114, s[6:7]
	v_cndmask_b32_e64 v175, v243, v115, s[6:7]
	v_cndmask_b32_e64 v168, v116, v243, s[10:11]
	v_cndmask_b32_e64 v169, v117, v243, s[14:15]
	v_cndmask_b32_e64 v164, v118, v243, s[18:19]
	v_max3_f32 v2, v174, v175, v168
	s_waitcnt lgkmcnt(0)
	v_mfma_f32_32x32x16_bf16 v[130:145], v[194:197], v[190:193], v[130:145]
	v_cndmask_b32_e64 v165, v119, v243, s[22:23]
	v_max3_f32 v2, v2, v169, v164
	v_cndmask_b32_e64 v124, v124, v243, s[44:45]
	v_cndmask_b32_e64 v125, v125, v243, s[48:49]
	v_cndmask_b32_e64 v115, v129, v243, s[64:65]
	v_cndmask_b32_e64 v114, v128, v243, s[60:61]
	v_max_f32_e32 v128, v115, v115
	s_nop 4
	v_cndmask_b32_e64 v172, v130, v243, s[4:5]
	v_cndmask_b32_e64 v173, v131, v243, s[8:9]
	v_cndmask_b32_e64 v170, v132, v243, s[12:13]
	v_cndmask_b32_e64 v171, v133, v243, s[16:17]
	v_cndmask_b32_e64 v166, v134, v243, s[20:21]
	v_cndmask_b32_e64 v134, v120, v243, s[26:27]
	v_cndmask_b32_e64 v120, v126, v243, s[52:53]
	v_max3_f32 v126, v172, v173, v170
	v_cndmask_b32_e64 v167, v135, v243, s[24:25]
	v_cndmask_b32_e64 v136, v136, v243, s[28:29]
	v_max3_f32 v126, v126, v171, v166
	v_cndmask_b32_e64 v135, v121, v243, s[30:31]
	v_cndmask_b32_e64 v137, v137, v243, s[34:35]
	v_cndmask_b32_e64 v130, v122, v243, s[36:37]
	v_cndmask_b32_e64 v132, v138, v243, s[38:39]
	v_max3_f32 v2, v2, v165, v134
	v_max3_f32 v126, v126, v167, v136
	v_cndmask_b32_e64 v131, v123, v243, s[40:41]
	v_cndmask_b32_e64 v133, v139, v243, s[42:43]
	v_cndmask_b32_e64 v122, v140, v243, s[46:47]
	v_max3_f32 v2, v2, v135, v130
	v_max3_f32 v126, v126, v137, v132
	v_cndmask_b32_e64 v123, v141, v243, s[50:51]
	v_cndmask_b32_e64 v116, v142, v243, s[54:55]
	v_cndmask_b32_e64 v119, v145, v243, s[66:67]
	v_max3_f32 v2, v2, v131, v124
	v_max3_f32 v126, v126, v133, v122
	v_cndmask_b32_e64 v121, v127, v243, s[56:57]
	v_cndmask_b32_e64 v117, v143, v243, s[58:59]
	v_cndmask_b32_e64 v118, v144, v243, s[62:63]
	v_max3_f32 v2, v2, v125, v120
	v_max3_f32 v126, v126, v123, v116
	v_max_f32_e32 v127, v119, v119
	v_max3_f32 v2, v2, v121, v114
	v_max3_f32 v126, v126, v117, v118
	v_max_f32_e32 v127, v128, v127
	v_max3_f32 v2, v2, v126, v127
	ds_bpermute_b32 v126, v217, v2
	s_waitcnt lgkmcnt(0)
	v_max_f32_e32 v126, v126, v126
	v_max_f32_e32 v126, v2, v126
	s_cbranch_vccz .LBB0_898
	v_readlane_b32 s56, v255, 12
	v_cmp_lt_f32_e32 vcc, s0, v126
	s_mov_b64 s[2:3], 0
	s_mov_b64 s[0:1], 0
	v_readlane_b32 s57, v255, 13
	s_mov_b32 s55, 0xda24260
	s_cbranch_vccz .LBB0_893
	v_max_f32_e32 v2, v126, v126
	v_max_f32_e32 v2, 0, v2
	s_mov_b64 s[0:1], -1
